# lever 7 (DPP instead of LDS round trips): top-k counting-step wave sum on DPP + readlane; conversion window C cut to 1 item per wave on the idle workgroups, prologue converts 2784 MoE items
# speedup vs baseline: 1.0057x; 1.0053x over previous
.LBB0_15:
	s_load_dwordx16 s[4:19], s[0:1], 0x0
	s_waitcnt lgkmcnt(0)
	v_writelane_b32 v253, s4, 34
	s_nop 1
	v_writelane_b32 v253, s5, 35
	v_writelane_b32 v253, s6, 36
	v_writelane_b32 v253, s7, 37
	v_writelane_b32 v253, s8, 38
	v_writelane_b32 v253, s9, 39
	v_writelane_b32 v253, s10, 40
	v_writelane_b32 v253, s11, 41
	v_writelane_b32 v253, s12, 42
	v_writelane_b32 v253, s13, 43
	v_writelane_b32 v253, s14, 44
	v_writelane_b32 v253, s15, 45
	v_writelane_b32 v253, s16, 46
	v_writelane_b32 v253, s17, 47
	v_writelane_b32 v253, s18, 48
	v_writelane_b32 v253, s19, 49
	s_load_dwordx16 s[4:19], s[0:1], 0x40
	s_lshr_b32 s0, s33, 6
	s_waitcnt lgkmcnt(0)
	v_writelane_b32 v253, s4, 50
	s_nop 1
	v_writelane_b32 v253, s5, 51
	v_writelane_b32 v253, s6, 52
	v_writelane_b32 v253, s7, 53
	v_writelane_b32 v253, s8, 54
	v_writelane_b32 v253, s9, 55
	v_writelane_b32 v253, s10, 56
	v_writelane_b32 v253, s11, 57
	v_writelane_b32 v253, s12, 58
	v_writelane_b32 v253, s13, 59
	v_writelane_b32 v253, s14, 60
	v_writelane_b32 v253, s15, 61
	v_writelane_b32 v253, s16, 62
	v_writelane_b32 v254, s18, 0
	v_writelane_b32 v253, s17, 63
	v_writelane_b32 v254, s19, 1
	v_writelane_b32 v254, s0, 2
	v_readlane_b32 s0, v253, 4
	v_readlane_b32 s1, v253, 5
	s_mov_b64 s[4:5], s[0:1]
	s_cmp_gt_i32 s4, 0
	v_readlane_b32 s2, v253, 6
	v_readlane_b32 s3, v253, 7
	s_cselect_b64 s[0:1], -1, 0
	s_cmp_lt_i32 s5, 1
	s_cselect_b64 s[2:3], -1, 0
	s_or_b64 s[0:1], s[0:1], s[2:3]
	s_and_b64 vcc, exec, s[0:1]
	s_cbranch_vccnz .LBB0_143
	v_readlane_b32 s0, v253, 3
	s_lshl_b32 s0, s0, 3
	v_readlane_b32 s1, v254, 2
	s_add_i32 s14, s0, s1
	s_lshl_b32 s15, s70, 3
	s_cmpk_eq_i32 s70, 0x100
	s_movk_i32 s0, 0x2800
	s_cselect_b32 s16, s0, 0x19d20
	v_readlane_b32 s0, v253, 8
	v_readlane_b32 s2, v253, 10
	v_readlane_b32 s3, v253, 11
	v_readlane_b32 s6, v253, 14
	v_readlane_b32 s7, v253, 15
	s_mov_b64 s[2:3], s[6:7]
	s_cmp_ge_i32 s14, s16
	v_mbcnt_lo_u32_b32 v1, -1, 0
	v_mbcnt_hi_u32_b32 v1, -1, v1
	v_readlane_b32 s1, v253, 9
	v_and_b32_e32 v0, 63, v1
	v_readlane_b32 s4, v253, 12
	v_readlane_b32 s5, v253, 13
	s_cbranch_scc1 .LBB0_38
	v_readlane_b32 s0, v254, 2
	s_lshl_b32 s0, s0, 14
	s_add_i32 s0, s0, 0
	s_add_u32 s17, s2, 0x31a00000
	s_addc_u32 s18, s3, 0
	s_add_u32 s19, s2, 0x21a00000
	s_addc_u32 s20, s3, 0
	s_add_u32 s21, s2, 0x21600000
	s_addc_u32 s22, s3, 0
	s_add_u32 s23, s2, 0x20900000
	s_addc_u32 s24, s3, 0
	v_lshrrev_b32_e32 v24, 3, v0
	v_and_b32_e32 v4, 7, v1
	s_add_u32 s25, s2, 0x20500000
	v_lshlrev_b32_e32 v14, 10, v24
	v_lshl_add_u32 v5, v4, 4, s0
	v_mul_u32_u24_e32 v6, 0x84, v24
	s_addc_u32 s26, s3, 0
	v_lshlrev_b32_e32 v2, 2, v4
	v_or_b32_e32 v16, 0x2000, v14
	v_or_b32_e32 v18, 0x4000, v14
	v_or_b32_e32 v20, 0x6000, v14
	v_lshlrev_b32_e32 v12, 3, v4
	v_mul_u32_u24_e32 v4, 0x420, v4
	v_lshlrev_b32_e32 v7, 2, v24
	s_add_u32 s27, s2, 0x1fc00000
	v_add_u32_e32 v26, v5, v6
	s_mov_b32 s1, 0
	v_mov_b32_e32 v3, 0
	v_add3_u32 v25, s0, v4, v7
	s_addc_u32 s28, s3, 0
	s_mov_b32 s29, 0x30000
	v_add_u32_e32 v27, 0x420, v26
	v_add_u32_e32 v28, 0x428, v26
	v_add_u32_e32 v29, 0x840, v26
	v_add_u32_e32 v30, 0x848, v26
	v_add_u32_e32 v31, 0xc60, v26
	v_add_u32_e32 v32, 0xc68, v26
	v_add_u32_e32 v33, 0x1080, v26
	v_add_u32_e32 v34, 0x1088, v26
	v_add_u32_e32 v35, 0x14a0, v26
	v_add_u32_e32 v36, 0x14a8, v26
	v_add_u32_e32 v37, 0x18c0, v26
	v_add_u32_e32 v38, 0x18c8, v26
	v_add_u32_e32 v39, 0x1ce0, v26
	v_add_u32_e32 v40, 0x1ce8, v26
	s_movk_i32 s30, 0x7fff
	s_mov_b32 s31, 0xffff0000
	s_movk_i32 s34, 0x2400
	v_lshlrev_b32_e32 v2, 2, v2
	v_lshlrev_b32_e32 v4, 2, v14
	v_lshlrev_b32_e32 v6, 2, v16
	v_lshlrev_b32_e32 v8, 2, v18
	v_lshlrev_b32_e32 v10, 2, v20
	v_lshlrev_b32_e32 v12, 1, v12
	v_lshlrev_b32_e32 v14, 1, v14
	v_lshlrev_b32_e32 v16, 1, v16
	v_lshlrev_b32_e32 v18, 1, v18
	v_lshlrev_b32_e32 v20, 1, v20
	s_mov_b32 s35, s14
	s_branch .LBB0_19

.LBB0_322:
	s_cmpk_gt_i32 s3, 0xe7
	v_readlane_b32 s2, v254, 39
	s_cselect_b64 s[0:1], -1, 0
	v_readlane_b32 s3, v254, 40
	s_and_b64 s[0:1], s[2:3], s[0:1]
	s_andn2_b64 vcc, exec, s[0:1]
	s_cbranch_vccnz .LBB0_336
	v_readlane_b32 s2, v254, 59
	s_cmp_eq_u32 s2, 0
	s_mov_b32 s0, 0x88a0
	s_cselect_b32 s0, 0xae0, s0
	s_cmp_gt_u32 s2, 1
	s_cselect_b32 s1, 0x74c0, 0
	s_add_i32 s0, s0, s1
	s_cmp_eq_u32 s2, 3
	s_cselect_b32 s1, 0x7dc0, 0
	s_add_i32 s2, s0, s1
	v_readlane_b32 s0, v255, 0
	s_mul_i32 s3, s0, 72
	s_add_i32 s16, s2, 0x6c0
	s_min_u32 s16, s16, 0x18000
	s_add_i32 s2, s2, s56
	v_readlane_b32 s4, v253, 8
	s_add_i32 s14, s2, s3
	v_readlane_b32 s10, v253, 14
	v_readlane_b32 s11, v253, 15
	s_add_i32 s14, s14, 0xffffbec0
	s_mov_b64 s[0:1], s[10:11]
	s_cmp_ge_i32 s14, s16
	v_readlane_b32 s5, v253, 9
	v_readlane_b32 s6, v253, 10
	v_readlane_b32 s7, v253, 11
	v_readlane_b32 s8, v253, 12
	v_readlane_b32 s9, v253, 13
	v_mbcnt_lo_u32_b32 v0, -1, 0
	v_mbcnt_hi_u32_b32 v0, -1, v0
	s_cbranch_scc1 .LBB0_336
	s_mul_hi_i32 s2, s14, 0x2aaaaaab
	s_lshr_b32 s3, s2, 31
	s_ashr_i32 s2, s2, 12
	s_add_i32 s3, s2, s3
	s_mul_i32 s2, s3, 0x6000
	s_sub_i32 s19, s14, s2
	s_lshl_b32 s15, s19, 5
	s_lshl_b32 s3, s3, 4
	s_bfe_u32 s4, s19, 0x40009
	s_bfe_u32 s18, s19, 0x40005
	s_and_b32 s2, s15, 0x3e0
	s_ashr_i32 s17, s19, 13
	s_or_b32 s8, s4, s3
	s_cmp_gt_i32 s17, 1
	s_mov_b64 s[12:13], -1
	s_cbranch_scc0 .LBB0_326
	s_ashr_i32 s9, s8, 31
	v_readlane_b32 s20, v253, 8
	s_lshl_b64 s[4:5], s[8:9], 22
	v_readlane_b32 s22, v253, 10
	v_readlane_b32 s23, v253, 11
	s_add_u32 s3, s22, s4
	s_addc_u32 s4, s23, s5
	s_lshl_b32 s30, s18, 6
	s_lshl_b32 s5, s18, 18
	s_add_u32 s5, s3, s5
	s_addc_u32 s4, s4, 0
	s_lshl_b32 s6, s2, 2
	s_add_u32 s6, s5, s6
	s_addc_u32 s7, s4, 0
	s_lshl_b64 s[4:5], s[8:9], 21
	s_add_u32 s4, s0, s4
	s_addc_u32 s5, s1, s5
	s_add_u32 s4, s4, 0x31a00000
	v_readlane_b32 s21, v253, 9
	v_readlane_b32 s24, v253, 12
	v_readlane_b32 s25, v253, 13
	v_readlane_b32 s26, v253, 14
	v_readlane_b32 s27, v253, 15
	s_mov_b32 s3, s31
	s_addc_u32 s5, s5, 0
	s_mov_b64 s[12:13], 0

.LBB0_658:
	v_readlane_b32 s0, v255, 0
	s_cmpk_gt_i32 s0, 0xc7
	v_readlane_b32 s2, v254, 39
	s_cselect_b64 s[0:1], -1, 0
	v_readlane_b32 s3, v254, 40
	s_and_b64 s[0:1], s[2:3], s[0:1]
	s_andn2_b64 vcc, exec, s[0:1]
	s_cbranch_vccnz .LBB0_672
	v_readlane_b32 s1, v254, 59
	s_cmp_eq_u32 s1, 0
	s_mov_b32 s0, 0x88a0
	s_cselect_b32 s0, 0xae0, s0
	s_cmp_gt_u32 s1, 1
	s_cselect_b32 s1, 0x74c0, 0
	s_add_i32 s8, s0, s1
	v_readlane_b32 s0, v255, 0
	v_readlane_b32 s12, v253, 8
	s_mul_i32 s2, s0, 72
	v_readlane_b32 s14, v253, 10
	s_add_i32 s3, s8, s56
	s_add_i32 s14, s3, s2
	v_readlane_b32 s18, v253, 14
	v_readlane_b32 s19, v253, 15
	s_add_i32 s14, s14, 0xffffc7c0
	s_add_i32 s8, s8, 0xfc0
	s_min_u32 s8, s8, 0x18000
	s_mov_b64 s[0:1], s[18:19]
	s_cmp_ge_i32 s14, s8
	v_readlane_b32 s13, v253, 9
	v_readlane_b32 s15, v253, 11
	v_readlane_b32 s16, v253, 12
	v_readlane_b32 s17, v253, 13
	v_mbcnt_lo_u32_b32 v0, -1, 0
	v_mbcnt_hi_u32_b32 v0, -1, v0
	s_cbranch_scc1 .LBB0_672
	s_mul_hi_i32 s2, s14, 0x2aaaaaab
	s_lshr_b32 s3, s2, 31
	s_ashr_i32 s2, s2, 12
	s_add_i32 s3, s2, s3
	s_mul_i32 s2, s3, 0x6000
	s_sub_i32 s17, s14, s2
	s_lshl_b32 s9, s17, 5
	s_lshl_b32 s3, s3, 4
	s_bfe_u32 s4, s17, 0x40009
	s_bfe_u32 s16, s17, 0x40005
	s_and_b32 s2, s9, 0x3e0
	s_ashr_i32 s15, s17, 13
	s_or_b32 s10, s4, s3
	s_cmp_gt_i32 s15, 1
	s_mov_b64 s[12:13], -1
	s_cbranch_scc0 .LBB0_662
	s_ashr_i32 s11, s10, 31
	v_readlane_b32 s20, v253, 8
	s_lshl_b64 s[4:5], s[10:11], 22
	v_readlane_b32 s22, v253, 10
	v_readlane_b32 s23, v253, 11
	s_add_u32 s3, s22, s4
	s_addc_u32 s4, s23, s5
	s_lshl_b32 s30, s16, 6
	s_lshl_b32 s5, s16, 18
	s_add_u32 s5, s3, s5
	s_addc_u32 s4, s4, 0
	s_lshl_b32 s6, s2, 2
	s_add_u32 s6, s5, s6
	s_addc_u32 s7, s4, 0
	s_lshl_b64 s[4:5], s[10:11], 21
	s_add_u32 s4, s0, s4
	s_addc_u32 s5, s1, s5
	s_add_u32 s4, s4, 0x31a00000
	v_readlane_b32 s21, v253, 9
	v_readlane_b32 s24, v253, 12
	v_readlane_b32 s25, v253, 13
	v_readlane_b32 s26, v253, 14
	v_readlane_b32 s27, v253, 15
	s_mov_b32 s3, s31
	s_addc_u32 s5, s5, 0
	s_mov_b64 s[12:13], 0

.LBB0_1122:
	v_readlane_b32 s0, v254, 59
	s_cmp_lg_u32 s0, 3
	v_readlane_b32 s2, v254, 39
	s_cselect_b64 s[0:1], -1, 0
	v_readlane_b32 s3, v254, 40
	s_and_b64 s[0:1], s[2:3], s[0:1]
	s_cmp_gt_i32 s6, 31
	s_cselect_b64 s[2:3], -1, 0
	s_and_b64 s[0:1], s[0:1], s[2:3]
	s_andn2_b64 vcc, exec, s[0:1]
	s_cbranch_vccnz .LBB0_1136
	v_readlane_b32 s0, v255, 1
	v_readlane_b32 s1, v255, 2
	s_and_b64 s[0:1], s[0:1], exec
	s_movk_i32 s0, 0xfc0
	v_readlane_b32 s2, v254, 59
	s_cselect_b32 s0, s0, 0x6c0
	s_cmp_eq_u32 s2, 0
	s_mov_b32 s1, 0x88a0
	s_cselect_b32 s1, 0xae0, s1
	s_cmp_gt_u32 s2, 1
	s_cselect_b32 s2, 0x74c0, 0
	s_add_i32 s1, s1, s2
	s_add_i32 s14, s1, s0
	v_readlane_b32 s0, v255, 0
	s_mul_i32 s2, s0, 48
	s_add_i32 s3, s14, s56
	v_readlane_b32 s4, v253, 8
	s_add_i32 s12, s3, s2
	v_readlane_b32 s10, v253, 14
	v_readlane_b32 s11, v253, 15
	s_add_i32 s12, s12, 0xfffffa00
	s_add_i32 s14, s14, 0x2a00
	s_min_u32 s14, s14, 0x18000
	s_mov_b64 s[0:1], s[10:11]
	s_cmp_ge_i32 s12, s14
	v_readlane_b32 s5, v253, 9
	v_readlane_b32 s6, v253, 10
	v_readlane_b32 s7, v253, 11
	v_readlane_b32 s8, v253, 12
	v_readlane_b32 s9, v253, 13
	v_mbcnt_lo_u32_b32 v0, -1, 0
	v_mbcnt_hi_u32_b32 v0, -1, v0
	s_cbranch_scc1 .LBB0_1136
	s_mul_hi_i32 s2, s12, 0x2aaaaaab
	s_lshr_b32 s3, s2, 31
	s_ashr_i32 s2, s2, 12
	s_add_i32 s3, s2, s3
	s_mul_i32 s2, s3, 0x6000
	s_sub_i32 s17, s12, s2
	s_lshl_b32 s13, s17, 5
	s_lshl_b32 s3, s3, 4
	s_bfe_u32 s4, s17, 0x40009
	s_bfe_u32 s16, s17, 0x40005
	s_and_b32 s2, s13, 0x3e0
	s_ashr_i32 s15, s17, 13
	s_or_b32 s8, s4, s3
	s_cmp_gt_i32 s15, 1
	s_mov_b64 s[10:11], -1
	s_cbranch_scc0 .LBB0_1126
	s_ashr_i32 s9, s8, 31
	v_readlane_b32 s20, v253, 8
	s_lshl_b64 s[4:5], s[8:9], 22
	v_readlane_b32 s22, v253, 10
	v_readlane_b32 s23, v253, 11
	s_add_u32 s3, s22, s4
	s_addc_u32 s4, s23, s5
	s_lshl_b32 s30, s16, 6
	s_lshl_b32 s5, s16, 18
	s_add_u32 s5, s3, s5
	s_addc_u32 s4, s4, 0
	s_lshl_b32 s6, s2, 2
	s_add_u32 s6, s5, s6
	s_addc_u32 s7, s4, 0
	s_lshl_b64 s[4:5], s[8:9], 21
	s_add_u32 s4, s0, s4
	s_addc_u32 s5, s1, s5
	s_add_u32 s4, s4, 0x31a00000
	v_readlane_b32 s21, v253, 9
	v_readlane_b32 s24, v253, 12
	v_readlane_b32 s25, v253, 13
	v_readlane_b32 s26, v253, 14
	v_readlane_b32 s27, v253, 15
	s_mov_b32 s3, s31
	s_addc_u32 s5, s5, 0
	s_mov_b64 s[10:11], 0

.LBB0_1280:
	s_lshl_b32 s4, 1, s8
	s_or_b32 s10, s4, s68
	s_lshl_b32 s4, 2, s8
	s_or_b32 s11, s4, s68
	s_lshl_b32 s4, 3, s8
	v_cmp_le_u32_e32 vcc, s10, v26
	s_or_b32 s12, s4, s68
	s_and_b32 s4, s9, 8
	v_cndmask_b32_e64 v3, 0, 1, vcc
	v_cmp_gt_u32_e32 vcc, s11, v26
	s_lshl_b32 s4, s4, 2
	s_add_i32 s13, s4, 0
	v_cndmask_b32_e64 v27, v240, 0, vcc
	v_cmp_gt_u32_e32 vcc, s12, v26
	v_or_b32_e32 v3, v27, v3
	s_nop 0
	v_cndmask_b32_e64 v27, v241, 0, vcc
	v_cmp_gt_u32_e32 vcc, s11, v32
	s_nop 1
	v_cndmask_b32_e64 v29, v240, 0, vcc
	v_cmp_gt_u32_e32 vcc, s12, v32
	s_nop 1
	v_cndmask_b32_e64 v31, v241, 0, vcc
	v_cmp_gt_u32_e32 vcc, s11, v35
	s_nop 1
	v_cndmask_b32_e64 v33, v240, 0, vcc
	v_cmp_gt_u32_e32 vcc, s12, v35
	s_nop 1
	v_cndmask_b32_e64 v34, v241, 0, vcc
	v_cmp_gt_u32_e32 vcc, s11, v7
	s_nop 1
	v_cndmask_b32_e64 v38, v240, 0, vcc
	v_cmp_gt_u32_e32 vcc, s12, v7
	s_nop 1
	v_cndmask_b32_e64 v39, v241, 0, vcc
	v_cmp_gt_u32_e32 vcc, s11, v0
	s_nop 1
	v_cndmask_b32_e64 v40, v240, 0, vcc
	v_cmp_gt_u32_e32 vcc, s12, v0
	s_nop 1
	v_cndmask_b32_e64 v41, v241, 0, vcc
	v_cmp_gt_u32_e32 vcc, s11, v1
	s_nop 1
	v_cndmask_b32_e64 v42, v240, 0, vcc
	v_cmp_gt_u32_e32 vcc, s12, v1
	s_nop 1
	v_cndmask_b32_e64 v43, v241, 0, vcc
	v_cmp_le_u32_e32 vcc, s10, v36
	s_nop 1
	v_cndmask_b32_e64 v44, 0, 1, vcc
	v_cmp_gt_u32_e32 vcc, s11, v36
	s_nop 1
	v_cndmask_b32_e64 v45, v240, 0, vcc
	v_cmp_gt_u32_e32 vcc, s12, v36
	v_or_b32_e32 v44, v45, v44
	s_nop 0
	v_cndmask_b32_e64 v46, v241, 0, vcc
	v_cmp_le_u32_e32 vcc, s10, v37
	s_nop 1
	v_cndmask_b32_e64 v47, 0, 1, vcc
	v_cmp_gt_u32_e32 vcc, s11, v37
	s_nop 1
	v_cndmask_b32_e64 v48, v240, 0, vcc
	v_cmp_gt_u32_e32 vcc, s12, v37
	v_or_b32_e32 v47, v48, v47
	s_nop 0
	v_cndmask_b32_e64 v48, v241, 0, vcc
	v_cmp_le_u32_e32 vcc, s10, v1
	s_nop 1
	v_addc_co_u32_e32 v44, vcc, 0, v44, vcc
	v_cmp_le_u32_e32 vcc, s10, v0
	s_nop 1
	v_addc_co_u32_e32 v42, vcc, v44, v42, vcc
	v_cmp_le_u32_e32 vcc, s10, v7
	s_nop 1
	v_addc_co_u32_e32 v40, vcc, v42, v40, vcc
	v_cmp_le_u32_e32 vcc, s10, v35
	s_nop 1
	v_addc_co_u32_e32 v38, vcc, v40, v38, vcc
	v_cmp_le_u32_e32 vcc, s10, v32
	s_nop 1
	v_addc_co_u32_e32 v33, vcc, v38, v33, vcc
	v_add_u32_e32 v29, v33, v29
	v_add3_u32 v27, v29, v27, v31
	v_add3_u32 v27, v27, v34, v39
	v_add3_u32 v27, v27, v41, v43
	v_add3_u32 v27, v27, v46, v48
	v_add3_u32 v3, v27, v3, v47
	s_nop 1
	v_add_u32_dpp v3, v3, v3 quad_perm:[1,0,3,2] row_mask:0xf bank_mask:0xf
	s_nop 1
	v_add_u32_dpp v3, v3, v3 quad_perm:[2,3,0,1] row_mask:0xf bank_mask:0xf
	s_nop 1
	v_add_u32_dpp v3, v3, v3 row_ror:4 row_mask:0xf bank_mask:0xf
	s_nop 1
	v_add_u32_dpp v3, v3, v3 row_ror:8 row_mask:0xf bank_mask:0xf
	s_nop 1
	v_readlane_b32 s100, v3, 0
	v_readlane_b32 s101, v3, 16
	s_add_i32 s100, s100, s101
	v_readlane_b32 s101, v3, 32
	s_add_i32 s100, s100, s101
	v_readlane_b32 s101, v3, 48
	s_add_i32 s100, s100, s101
	v_mov_b32_e32 v3, s100
	v_mov_b32_e32 v27, 0
	s_and_saveexec_b64 s[4:5], s[44:45]
	s_cbranch_execz .LBB0_1279
	s_add_i32 s14, s13, s34
	v_add_u32_e32 v3, v3, v27
	v_mov_b32_e32 v27, s14
	ds_write_b32 v27, v3
	s_branch .LBB0_1279

.LBB0_1347:
	v_readlane_b32 s4, v254, 61
	s_cmpk_gt_i32 s4, 0x7f
	v_readlane_b32 s2, v254, 39
	s_cselect_b64 s[0:1], -1, 0
	v_readlane_b32 s3, v254, 40
	s_and_b64 s[0:1], s[2:3], s[0:1]
	s_andn2_b64 vcc, exec, s[0:1]
	s_mov_b32 s29, 0xffff0000
	s_movk_i32 s33, 0x7fff
	v_readlane_b32 s56, v255, 7
	s_cbranch_vccnz .LBB0_1361
	v_readlane_b32 s0, v255, 1
	v_readlane_b32 s1, v255, 2
	s_and_b64 s[0:1], s[0:1], exec
	s_movk_i32 s0, 0xfc0
	v_readlane_b32 s1, v254, 59
	s_cselect_b32 s2, s0, 0x6c0
	s_cmp_eq_u32 s1, 0
	s_mov_b32 s0, 0x88a0
	s_cselect_b32 s0, 0xae0, s0
	s_cmp_gt_u32 s1, 1
	s_cselect_b32 s1, 0x74c0, 0
	v_readlane_b32 s6, v255, 3
	s_add_i32 s3, s0, s1
	v_readlane_b32 s7, v255, 4
	s_and_b64 s[0:1], s[6:7], exec
	s_cselect_b32 s0, 0x7dc0, 0
	s_add_i32 s3, s3, s0
	s_and_b64 s[0:1], s[6:7], exec
	s_cselect_b32 s0, 0, 0x2a00
	s_add_i32 s0, s3, s0
	s_add_i32 s2, s0, s2
	s_cmpk_gt_i32 s4, 0x7f
	s_cselect_b32 s100, 0, 0
	s_cselect_b32 s3, 8, 8
	s_mov_b32 s101, 0xfffffc00
	s_cselect_b32 s101, 0xfffffc00, s101
	s_mul_i32 s3, s4, s3
	s_add_i32 s3, s3, s101
	v_readlane_b32 s4, v253, 8
	s_add_i32 s4, s2, s56
	s_add_i32 s12, s4, s3
	s_min_u32 s14, s2, 0x17c00
	v_readlane_b32 s10, v253, 14
	v_readlane_b32 s11, v253, 15
	s_nop 0
	s_add_i32 s14, s14, 0x400
	s_mov_b64 s[0:1], s[10:11]
	s_cmp_ge_i32 s12, s14
	v_readlane_b32 s5, v253, 9
	v_readlane_b32 s6, v253, 10
	v_readlane_b32 s7, v253, 11
	v_readlane_b32 s8, v253, 12
	v_readlane_b32 s9, v253, 13
	v_mbcnt_lo_u32_b32 v0, -1, 0
	v_mbcnt_hi_u32_b32 v0, -1, v0
	s_cbranch_scc1 .LBB0_1361
	s_mul_hi_i32 s2, s12, 0x2aaaaaab
	s_lshr_b32 s3, s2, 31
	s_ashr_i32 s2, s2, 12
	s_add_i32 s3, s2, s3
	s_mul_i32 s2, s3, 0x6000
	s_sub_i32 s17, s12, s2
	s_lshl_b32 s13, s17, 5
	s_lshl_b32 s3, s3, 4
	s_bfe_u32 s4, s17, 0x40009
	s_bfe_u32 s16, s17, 0x40005
	s_and_b32 s2, s13, 0x3e0
	s_ashr_i32 s15, s17, 13
	s_or_b32 s8, s4, s3
	s_cmp_gt_i32 s15, 1
	s_mov_b64 s[10:11], -1
	s_cbranch_scc0 .LBB0_1351
	s_ashr_i32 s9, s8, 31
	v_readlane_b32 s20, v253, 8
	s_lshl_b64 s[4:5], s[8:9], 22
	v_readlane_b32 s22, v253, 10
	v_readlane_b32 s23, v253, 11
	s_add_u32 s3, s22, s4
	s_addc_u32 s4, s23, s5
	s_lshl_b32 s30, s16, 6
	s_lshl_b32 s5, s16, 18
	s_add_u32 s5, s3, s5
	s_addc_u32 s4, s4, 0
	s_lshl_b32 s6, s2, 2
	s_add_u32 s6, s5, s6
	s_addc_u32 s7, s4, 0
	s_lshl_b64 s[4:5], s[8:9], 21
	s_add_u32 s4, s0, s4
	s_addc_u32 s5, s1, s5
	s_add_u32 s4, s4, 0x31a00000
	v_readlane_b32 s21, v253, 9
	v_readlane_b32 s24, v253, 12
	v_readlane_b32 s25, v253, 13
	v_readlane_b32 s26, v253, 14
	v_readlane_b32 s27, v253, 15
	s_mov_b32 s3, s31
	s_addc_u32 s5, s5, 0
	s_mov_b64 s[10:11], 0

.LBB0_1432:
	s_cmp_lg_u32 s1, 3
	v_readlane_b32 s2, v254, 39
	s_cselect_b64 s[0:1], -1, 0
	v_readlane_b32 s3, v254, 40
	s_and_b64 s[0:1], s[2:3], s[0:1]
	s_cmpk_gt_i32 s4, 0x7f
	s_cselect_b64 s[2:3], -1, 0
	s_and_b64 s[0:1], s[0:1], s[2:3]
	s_andn2_b64 vcc, exec, s[0:1]
	s_cbranch_vccnz .LBB0_1446
	v_readlane_b32 s0, v255, 1
	v_readlane_b32 s1, v255, 2
	s_and_b64 s[0:1], s[0:1], exec
	s_movk_i32 s0, 0xfc0
	v_readlane_b32 s2, v254, 59
	s_cselect_b32 s0, s0, 0x6c0
	s_cmp_eq_u32 s2, 0
	s_mov_b32 s1, 0x88a0
	s_cselect_b32 s1, 0xae0, s1
	s_cmp_gt_u32 s2, 1
	s_cselect_b32 s2, 0x74c0, 0
	s_add_i32 s1, s1, s2
	s_add_i32 s14, s1, s0
	v_readlane_b32 s0, v255, 0
	s_mul_i32 s2, s0, 56
	s_add_i32 s3, s14, s56
	v_readlane_b32 s4, v253, 8
	s_add_i32 s12, s3, s2
	v_readlane_b32 s10, v253, 14
	v_readlane_b32 s11, v253, 15
	s_add_i32 s12, s12, 0x1200
	s_add_i32 s14, s14, 0x4a00
	s_min_u32 s14, s14, 0x18000
	s_mov_b64 s[0:1], s[10:11]
	s_cmp_ge_i32 s12, s14
	v_readlane_b32 s5, v253, 9
	v_readlane_b32 s6, v253, 10
	v_readlane_b32 s7, v253, 11
	v_readlane_b32 s8, v253, 12
	v_readlane_b32 s9, v253, 13
	v_mbcnt_lo_u32_b32 v0, -1, 0
	v_mbcnt_hi_u32_b32 v0, -1, v0
	s_cbranch_scc1 .LBB0_1446
	s_mul_hi_i32 s2, s12, 0x2aaaaaab
	s_lshr_b32 s3, s2, 31
	s_ashr_i32 s2, s2, 12
	s_add_i32 s3, s2, s3
	s_mul_i32 s2, s3, 0x6000
	s_sub_i32 s17, s12, s2
	s_lshl_b32 s13, s17, 5
	s_lshl_b32 s3, s3, 4
	s_bfe_u32 s4, s17, 0x40009
	s_bfe_u32 s16, s17, 0x40005
	s_and_b32 s2, s13, 0x3e0
	s_ashr_i32 s15, s17, 13
	s_or_b32 s8, s4, s3
	s_cmp_gt_i32 s15, 1
	s_mov_b64 s[10:11], -1
	s_cbranch_scc0 .LBB0_1436
	s_ashr_i32 s9, s8, 31
	v_readlane_b32 s20, v253, 8
	s_lshl_b64 s[4:5], s[8:9], 22
	v_readlane_b32 s22, v253, 10
	v_readlane_b32 s23, v253, 11
	s_add_u32 s3, s22, s4
	s_addc_u32 s4, s23, s5
	s_lshl_b32 s30, s16, 6
	s_lshl_b32 s5, s16, 18
	s_add_u32 s5, s3, s5
	s_addc_u32 s4, s4, 0
	s_lshl_b32 s6, s2, 2
	s_add_u32 s6, s5, s6
	s_addc_u32 s7, s4, 0
	s_lshl_b64 s[4:5], s[8:9], 21
	s_add_u32 s4, s0, s4
	s_addc_u32 s5, s1, s5
	s_add_u32 s4, s4, 0x31a00000
	v_readlane_b32 s21, v253, 9
	v_readlane_b32 s24, v253, 12
	v_readlane_b32 s25, v253, 13
	v_readlane_b32 s26, v253, 14
	v_readlane_b32 s27, v253, 15
	s_mov_b32 s3, s31
	s_addc_u32 s5, s5, 0
	s_mov_b64 s[10:11], 0

.LBB0_1513:
	s_cmp_lg_u32 s1, 3
	v_readlane_b32 s2, v254, 39
	s_cselect_b64 s[0:1], -1, 0
	v_readlane_b32 s3, v254, 40
	s_and_b64 s[0:1], s[2:3], s[0:1]
	s_cmp_gt_i32 s4, 63
	s_cselect_b64 s[2:3], -1, 0
	s_and_b64 s[0:1], s[0:1], s[2:3]
	s_andn2_b64 vcc, exec, s[0:1]
	s_cbranch_vccnz .LBB0_1527
	v_readlane_b32 s0, v255, 1
	v_readlane_b32 s1, v255, 2
	s_and_b64 s[0:1], s[0:1], exec
	s_movk_i32 s0, 0xfc0
	v_readlane_b32 s2, v254, 59
	s_cselect_b32 s0, s0, 0x6c0
	s_cmp_eq_u32 s2, 0
	s_mov_b32 s1, 0x88a0
	s_cselect_b32 s1, 0xae0, s1
	s_cmp_gt_u32 s2, 1
	s_cselect_b32 s2, 0x74c0, 0
	s_add_i32 s1, s1, s2
	s_add_i32 s14, s1, s0
	s_mul_i32 s2, s4, 48
	s_add_i32 s3, s14, s56
	v_readlane_b32 s4, v253, 8
	s_add_i32 s12, s3, s2
	v_readlane_b32 s10, v253, 14
	v_readlane_b32 s11, v253, 15
	s_add_i32 s12, s12, 0x3e00
	s_add_i32 s14, s14, 0x6e00
	s_min_u32 s14, s14, 0x18000
	s_mov_b64 s[0:1], s[10:11]
	s_cmp_ge_i32 s12, s14
	v_readlane_b32 s5, v253, 9
	v_readlane_b32 s6, v253, 10
	v_readlane_b32 s7, v253, 11
	v_readlane_b32 s8, v253, 12
	v_readlane_b32 s9, v253, 13
	v_mbcnt_lo_u32_b32 v0, -1, 0
	v_mbcnt_hi_u32_b32 v0, -1, v0
	s_cbranch_scc1 .LBB0_1527
	s_mul_hi_i32 s2, s12, 0x2aaaaaab
	s_lshr_b32 s3, s2, 31
	s_ashr_i32 s2, s2, 12
	s_add_i32 s3, s2, s3
	s_mul_i32 s2, s3, 0x6000
	s_sub_i32 s17, s12, s2
	s_lshl_b32 s13, s17, 5
	s_lshl_b32 s3, s3, 4
	s_bfe_u32 s4, s17, 0x40009
	s_bfe_u32 s16, s17, 0x40005
	s_and_b32 s2, s13, 0x3e0
	s_ashr_i32 s15, s17, 13
	s_or_b32 s8, s4, s3
	s_cmp_gt_i32 s15, 1
	s_mov_b64 s[10:11], -1
	s_cbranch_scc0 .LBB0_1517
	s_ashr_i32 s9, s8, 31
	v_readlane_b32 s20, v253, 8
	s_lshl_b64 s[4:5], s[8:9], 22
	v_readlane_b32 s22, v253, 10
	v_readlane_b32 s23, v253, 11
	s_add_u32 s3, s22, s4
	s_addc_u32 s4, s23, s5
	s_lshl_b32 s30, s16, 6
	s_lshl_b32 s5, s16, 18
	s_add_u32 s5, s3, s5
	s_addc_u32 s4, s4, 0
	s_lshl_b32 s6, s2, 2
	s_add_u32 s6, s5, s6
	s_addc_u32 s7, s4, 0
	s_lshl_b64 s[4:5], s[8:9], 21
	s_add_u32 s4, s0, s4
	s_addc_u32 s5, s1, s5
	s_add_u32 s4, s4, 0x31a00000
	v_readlane_b32 s21, v253, 9
	v_readlane_b32 s24, v253, 12
	v_readlane_b32 s25, v253, 13
	v_readlane_b32 s26, v253, 14
	v_readlane_b32 s27, v253, 15
	s_mov_b32 s3, s31
	s_addc_u32 s5, s5, 0
	s_mov_b64 s[10:11], 0
